# stack28 = stack23 + kernel head: all kernel-argument lines requested with the first scalar loads (the second dependent scalar-cache miss removed)
# baseline (speedup 1.0000x reference)
; #define LAS __attribute__((address_space(3)))
; DEVINL void xb_st0(unsigned* p) { __hip_atomic_store(p, 0u, __ATOMIC_RELAXED, __HIP_MEMORY_SCOPE_AGENT); }
; __global__ void __launch_bounds__(NTHR, 2) fwd_kernel(Params P) {
;     extern __shared__ __attribute__((aligned(16))) unsigned char smem[];
;     ...
;     cg::grid_group grid = cg::this_grid();
;     ...
;     volatile LAS unsigned* bst = (volatile LAS unsigned*)(smem + LDS_MISC + 2048);
;     if (threadIdx.x < 4) bst[threadIdx.x] = 0u;
;     __syncthreads();
;     if (blockIdx.x == 0 && threadIdx.x < 17) xb_st0(threadIdx.x < 16 ? &g_xbar[XB_XSUBI(NPHASE - 2, threadIdx.x)] : &g_xbar[XB_TOPI(NPHASE - 2)]);
;     const XcdBarrier xbar = xcd_barrier_post(g_xbar, bst);
_Z10fwd_kernel6Params:
	s_load_dwordx8 s[68:75], s[0:1], 0x80
	s_load_dwordx2 s[34:35], s[0:1], 0xa0
	s_load_dwordx4 s[76:79], s[0:1], 0xa8
	s_load_dwordx16 s[36:51], s[0:1], 0x40
	s_load_dword s52, s[0:1], 0x0
	s_load_dword s53, s[0:1], 0xc0
	s_mov_b32 s80, s2
	s_mov_b64 s[96:97], s[0:1]
	v_cmp_gt_u32_e64 s[2:3], 4, v0
	s_mov_b64 s[0:1], exec
	s_nop 0
	v_writelane_b32 v254, s2, 0
	s_nop 1
	v_writelane_b32 v254, s3, 1
	s_and_b64 s[2:3], s[0:1], s[2:3]
	s_mov_b64 exec, s[2:3]
	v_lshl_add_u32 v1, v0, 2, 0
	v_add_u32_e32 v1, 0x24800, v1
	v_mov_b32_e32 v2, 0
	ds_write_b32 v1, v2
	s_or_b64 exec, exec, s[0:1]
	s_cmp_eq_u32 s80, 0
	s_cselect_b64 s[0:1], -1, 0
	v_cmp_gt_u32_e32 vcc, 17, v0
	v_writelane_b32 v254, s0, 2
	s_and_b64 s[2:3], s[0:1], vcc
	s_waitcnt lgkmcnt(0)
	v_writelane_b32 v254, s1, 3
	s_barrier
	s_and_saveexec_b64 s[0:1], s[2:3]
	s_cbranch_execz .LBB0_4
	v_lshlrev_b32_e32 v2, 8, v0
	v_mov_b32_e32 v3, 0
	s_getpc_b64 s[2:3]
	s_add_u32 s2, s2, g_xbar@rel32@lo+28676
	s_addc_u32 s3, s3, g_xbar@rel32@hi+28684
	v_lshl_add_u64 v[4:5], s[2:3], 0, v[2:3]
	s_getpc_b64 s[2:3]
	s_add_u32 s2, s2, g_xbar@rel32@lo+33540
	s_addc_u32 s3, s3, g_xbar@rel32@hi+33548
	v_mov_b32_e32 v1, s3
	v_cmp_gt_u32_e32 vcc, 16, v0
	s_nop 1
	v_cndmask_b32_e32 v5, v1, v5, vcc
	v_mov_b32_e32 v1, s2
	v_cndmask_b32_e32 v4, v1, v4, vcc
	global_store_dword v[4:5], v3, off sc1
